# v13 + MoBA-C list counts kept in LDS (no per-item global count load) + seam-6 arrive without the unneeded L2 write-back; byte phase of later loops kept
# baseline (speedup 1.0000x reference)
.LBB0_1321:
	s_movk_i32 s0, 0x100
	v_cmp_gt_u32_e64 s[0:1], s0, v0
	v_mov_b32_e32 v1, 0
	s_and_saveexec_b64 s[4:5], s[0:1]
	s_cbranch_execz .LBB0_1325
	s_waitcnt lgkmcnt(0)
	v_lshlrev_b32_e32 v2, 2, v0
	v_mov_b32_e32 v3, 0
	v_lshl_add_u64 v[2:3], s[46:47], 0, v[2:3]
	v_add_co_u32_e32 v2, vcc, 0x1000, v2
	s_nop 1
	v_addc_co_u32_e32 v3, vcc, 0, v3, vcc
	global_load_dword v1, v[2:3], off sc1
	v_mbcnt_lo_u32_b32 v2, -1, 0
	v_mbcnt_hi_u32_b32 v2, -1, v2
	v_and_b32_e32 v3, 64, v2
	v_add_u32_e32 v4, -1, v2
	v_cmp_lt_i32_e32 vcc, v4, v3
	v_add_u32_e32 v5, -2, v2
	v_add_u32_e32 v6, -4, v2
	v_cndmask_b32_e32 v4, v4, v2, vcc
	v_lshlrev_b32_e32 v4, 2, v4
	v_cmp_lt_i32_e32 vcc, v5, v3
	v_add_u32_e32 v7, -8, v2
	v_add_u32_e32 v8, -16, v2
	v_cndmask_b32_e32 v5, v5, v2, vcc
	v_cmp_ne_u32_e32 vcc, 0, v248
	v_lshlrev_b32_e32 v5, 2, v5
	v_subrev_u32_e32 v9, 32, v2
	s_waitcnt vmcnt(0)
	v_lshlrev_b32_e32 v10, 2, v0
	v_add_u32_e32 v10, 0x21800, v10
	ds_write_b32 v10, v1
	s_nop 0
	v_add_u32_e32 v1, 0xff, v1
	v_ashrrev_i32_e32 v1, 8, v1
	ds_bpermute_b32 v4, v4, v1
	s_waitcnt lgkmcnt(0)
	v_cndmask_b32_e32 v4, 0, v4, vcc
	v_add_u32_e32 v4, v4, v1
	ds_bpermute_b32 v5, v5, v4
	v_cmp_lt_i32_e32 vcc, v6, v3
	s_nop 1
	v_cndmask_b32_e32 v6, v6, v2, vcc
	v_cmp_lt_u32_e32 vcc, 1, v248
	v_lshlrev_b32_e32 v6, 2, v6
	s_waitcnt lgkmcnt(0)
	v_cndmask_b32_e32 v5, 0, v5, vcc
	v_add_u32_e32 v4, v5, v4
	ds_bpermute_b32 v5, v6, v4
	v_cmp_lt_i32_e32 vcc, v7, v3
	s_nop 1
	v_cndmask_b32_e32 v6, v7, v2, vcc
	v_cmp_lt_u32_e32 vcc, 3, v248
	v_lshlrev_b32_e32 v6, 2, v6
	s_waitcnt lgkmcnt(0)
	v_cndmask_b32_e32 v5, 0, v5, vcc
	v_add_u32_e32 v4, v5, v4
	ds_bpermute_b32 v5, v6, v4
	v_cmp_lt_i32_e32 vcc, v8, v3
	s_nop 1
	v_cndmask_b32_e32 v6, v8, v2, vcc
	v_cmp_lt_u32_e32 vcc, 7, v248
	v_lshlrev_b32_e32 v6, 2, v6
	s_waitcnt lgkmcnt(0)
	v_cndmask_b32_e32 v5, 0, v5, vcc
	v_add_u32_e32 v4, v5, v4
	ds_bpermute_b32 v5, v6, v4
	v_cmp_lt_i32_e32 vcc, v9, v3
	s_nop 1
	v_cndmask_b32_e32 v2, v9, v2, vcc
	v_cmp_lt_u32_e32 vcc, 15, v248
	v_lshlrev_b32_e32 v2, 2, v2
	s_waitcnt lgkmcnt(0)
	v_cndmask_b32_e32 v3, 0, v5, vcc
	v_add_u32_e32 v3, v3, v4
	ds_bpermute_b32 v2, v2, v3
	v_cmp_lt_u32_e32 vcc, 31, v248
	s_waitcnt lgkmcnt(0)
	s_nop 0
	v_cndmask_b32_e32 v2, 0, v2, vcc
	v_add_u32_e32 v2, v2, v3
	v_cmp_eq_u32_e32 vcc, 63, v248
	s_and_saveexec_b64 s[6:7], vcc
	s_lshl_b32 s8, s91, 2
	s_add_i32 s8, s8, 0
	s_add_i32 s8, s8, 0x21410
	v_mov_b32_e32 v3, s8
	ds_write_b32 v3, v2
	s_or_b64 exec, exec, s[6:7]
	v_lshl_add_u32 v3, v0, 2, 0
	v_sub_u32_e32 v2, v2, v1
	v_add_u32_e32 v3, 0x21000, v3
	ds_write_b32 v3, v2

.LBB0_1750:
	s_or_b64 exec, exec, s[4:5]
	s_waitcnt vmcnt(0)
	v_readfirstlane_b32 s4, v4
	s_nop 1
	v_add3_u32 v3, s4, v3, 1
	v_cmp_eq_u32_e32 vcc, v3, v2
	s_and_b64 exec, exec, vcc
	s_cbranch_execz .LBB0_1786
	s_mov_b64 s[4:5], exec
	s_waitcnt vmcnt(0)
	v_mbcnt_lo_u32_b32 v2, s4, 0
	v_mbcnt_hi_u32_b32 v2, s5, v2
	v_cmp_eq_u32_e32 vcc, 0, v2
	s_and_saveexec_b64 s[6:7], vcc
	s_cbranch_execz .LBB0_1753
	s_bcnt1_i32_b64 s4, s[4:5]
	v_mov_b32_e32 v3, 0xd000
	v_mov_b32_e32 v4, s4
	global_atomic_add v3, v3, v4, s[46:47] offset:2048 sc0
